# MoE-up GEMM: the four gathered-row index loads per unit issued together behind one wait instead of four dependent round trips
# speedup vs baseline: 1.0036x; 1.0036x over previous
.LBB0_1366:
	v_ashrrev_i32_e32 v1, 31, v2
	v_lshrrev_b32_e32 v1, 26, v1
	v_add_u32_e32 v1, v2, v1
	v_ashrrev_i32_e32 v4, 6, v1
	v_bfe_i32 v1, v2, 27, 1
	v_lshlrev_b32_e32 v10, 4, v2
	v_lshrrev_b32_e32 v1, 22, v1
	v_add_u32_e32 v1, v10, v1
	v_and_b32_e32 v1, 0xfffffc00, v1
	v_sub_u32_e32 v1, v10, v1
	v_lshrrev_b32_e32 v5, 4, v1
	v_bitop3_b32 v6, v5, v1, 32 bitop3:0x6c
	v_ashrrev_i32_e32 v5, 31, v6
	v_lshrrev_b32_e32 v5, 26, v5
	v_lshlrev_b32_e32 v1, 3, v4
	v_add_u32_e32 v5, v6, v5
	v_and_b32_e32 v1, -16, v1
	v_ashrrev_i32_e32 v5, 6, v5
	v_add_u32_e32 v1, v5, v1
	v_cmp_lt_i32_e32 vcc, v1, v7
	v_mov_b32_e32 v8, 0
	v_mov_b32_e32 v9, 0
	s_and_saveexec_b64 s[0:1], vcc
	v_add_u32_e32 v12, v3, v1
	v_readlane_b32 s2, v253, 36
	v_ashrrev_i32_e32 v13, 31, v12
	v_readlane_b32 s3, v253, 37
	s_nop 1
	v_lshl_add_u64 v[12:13], v[12:13], 2, s[2:3]
	global_load_dword v9, v[12:13], off
	s_or_b64 exec, exec, s[0:1]
	v_add_u32_e32 v148, 0x80, v1
	v_cmp_lt_i32_e32 vcc, v148, v7
	s_and_saveexec_b64 s[0:1], vcc
	v_add_u32_e32 v12, v3, v148
	v_readlane_b32 s2, v253, 36
	v_ashrrev_i32_e32 v13, 31, v12
	v_readlane_b32 s3, v253, 37
	s_nop 1
	v_lshl_add_u64 v[12:13], v[12:13], 2, s[2:3]
	global_load_dword v8, v[12:13], off
	s_or_b64 exec, exec, s[0:1]
	v_add_u32_e32 v10, 0x2000, v10
	v_ashrrev_i32_e32 v11, 31, v10
	v_lshrrev_b32_e32 v11, 22, v11
	v_add_u32_e32 v11, v10, v11
	v_ashrrev_i32_e32 v11, 10, v11
	v_mul_i32_i24_e32 v12, 0x400, v11
	v_sub_u32_e32 v10, v10, v12
	v_lshrrev_b32_e32 v12, 4, v10
	v_bitop3_b32 v13, v12, v10, 32 bitop3:0x6c
	v_ashrrev_i32_e32 v12, 31, v13
	v_lshrrev_b32_e32 v12, 26, v12
	v_lshlrev_b32_e32 v10, 3, v11
	v_add_u32_e32 v12, v13, v12
	v_and_b32_e32 v10, -16, v10
	v_ashrrev_i32_e32 v12, 6, v12
	v_add_u32_e32 v149, v12, v10
	v_cmp_lt_i32_e32 vcc, v149, v7
	v_mov_b32_e32 v10, 0
	v_mov_b32_e32 v14, 0
	s_and_saveexec_b64 s[0:1], vcc
	v_add_u32_e32 v14, v3, v149
	v_readlane_b32 s2, v253, 36
	v_ashrrev_i32_e32 v15, 31, v14
	v_readlane_b32 s3, v253, 37
	s_nop 1
	v_lshl_add_u64 v[14:15], v[14:15], 2, s[2:3]
	global_load_dword v14, v[14:15], off
	s_or_b64 exec, exec, s[0:1]
	v_add_u32_e32 v150, 0x80, v149
	v_mov_b32_e32 v16, 0
	v_cmp_lt_i32_e32 vcc, v150, v7
	s_and_saveexec_b64 s[0:1], vcc
	v_add_u32_e32 v16, v3, v150
	v_readlane_b32 s2, v253, 36
	v_ashrrev_i32_e32 v17, 31, v16
	v_readlane_b32 s3, v253, 37
	s_nop 1
	v_lshl_add_u64 v[16:17], v[16:17], 2, s[2:3]
	global_load_dword v16, v[16:17], off
	s_or_b64 exec, exec, s[0:1]
	s_waitcnt vmcnt(0)
	v_max_i32_e32 v9, 0, v9
	v_max_i32_e32 v8, 0, v8
	v_max_i32_e32 v14, 0, v14
	v_max_i32_e32 v16, 0, v16
	v_lshlrev_b32_e32 v9, 9, v9
	v_lshlrev_b32_e32 v8, 9, v8
	v_lshlrev_b32_e32 v14, 9, v14
	v_lshlrev_b32_e32 v16, 9, v16
	v_and_b32_e32 v9, 0x7ffffc00, v9
	v_and_b32_e32 v8, 0x7ffffc00, v8
	v_and_b32_e32 v14, 0x7ffffc00, v14
	v_and_b32_e32 v10, 0x7ffffc00, v16

.LBB0_1381:
	v_cndmask_b32_e64 v2, 0, 1, s[24:25]
	v_cmp_ne_u32_e64 s[0:1], 1, v2
	s_andn2_b64 vcc, exec, s[24:25]
	v_mov_b32_e32 v159, v140
	v_mov_b32_e32 v160, v136
	v_mov_b32_e32 v157, v142
	v_mov_b32_e32 v158, v138
	s_cbranch_vccnz .LBB0_1391
	v_readlane_b32 s26, v253, 36
	v_readlane_b32 s27, v253, 37
	v_mov_b32_e32 v2, 0
	v_mov_b32_e32 v3, 0
	v_cmp_lt_i32_e32 vcc, v1, v155
	s_and_saveexec_b64 s[18:19], vcc
	v_add_u32_e32 v4, v156, v1
	v_ashrrev_i32_e32 v5, 31, v4
	v_lshl_add_u64 v[4:5], v[4:5], 2, s[26:27]
	global_load_dword v3, v[4:5], off
	s_or_b64 exec, exec, s[18:19]
	v_cmp_lt_i32_e32 vcc, v148, v155
	s_and_saveexec_b64 s[18:19], vcc
	v_add_u32_e32 v4, v156, v148
	v_ashrrev_i32_e32 v5, 31, v4
	v_lshl_add_u64 v[4:5], v[4:5], 2, s[26:27]
	global_load_dword v2, v[4:5], off
	s_or_b64 exec, exec, s[18:19]
	v_mov_b32_e32 v4, 0
	v_mov_b32_e32 v5, 0
	v_cmp_lt_i32_e32 vcc, v149, v155
	s_and_saveexec_b64 s[18:19], vcc
	v_add_u32_e32 v6, v156, v149
	v_ashrrev_i32_e32 v7, 31, v6
	v_lshl_add_u64 v[6:7], v[6:7], 2, s[26:27]
	global_load_dword v5, v[6:7], off
	s_or_b64 exec, exec, s[18:19]
	v_cmp_lt_i32_e32 vcc, v150, v155
	s_and_saveexec_b64 s[18:19], vcc
	v_add_u32_e32 v6, v156, v150
	v_ashrrev_i32_e32 v7, 31, v6
	v_lshl_add_u64 v[6:7], v[6:7], 2, s[26:27]
	global_load_dword v4, v[6:7], off
	s_or_b64 exec, exec, s[18:19]
	s_waitcnt vmcnt(0)
	v_max_i32_e32 v3, 0, v3
	v_max_i32_e32 v2, 0, v2
	v_max_i32_e32 v5, 0, v5
	v_max_i32_e32 v4, 0, v4
	v_lshlrev_b32_e32 v3, 9, v3
	v_lshlrev_b32_e32 v2, 9, v2
	v_lshlrev_b32_e32 v5, 9, v5
	v_lshlrev_b32_e32 v4, 9, v4
	v_and_b32_e32 v3, 0x7ffffc00, v3
	v_and_b32_e32 v2, 0x7ffffc00, v2
	v_and_b32_e32 v5, 0x7ffffc00, v5
	v_and_b32_e32 v4, 0x7ffffc00, v4
	s_mov_b64 s[18:19], exec
